# biaspf
# speedup vs baseline: 1.0056x; 1.0007x over previous
.Lenc_skip2:
	s_or_b64 exec, exec, s[10:11]
	v_lshrrev_b32_e32 v45, 5, v0
	v_and_b32_e32 v54, 4, v45
	v_lshlrev_b32_e32 v45, 2, v54
	s_waitcnt vmcnt(0) lgkmcnt(0)
	s_barrier
	ds_read_b128 v[50:53], v45
	v_mov_b32_e32 v46, v1
	v_mov_b32_e32 v47, v1
	v_mov_b32_e32 v48, v1
	v_mov_b32_e32 v49, v1
	v_add_u32_e32 v3, s3, v54
	v_lshlrev_b32_e32 v3, 9, v3
	v_add_u32_e32 v3, v3, v2
	v_add_u32_e32 v3, 0x16000, v3
	ds_read_b128 v[56:59], v45 offset:32
	ds_read_b128 v[60:63], v45 offset:64
	ds_read_b128 v[64:67], v45 offset:96
	ds_read_b128 v[68:71], v45 offset:128
	s_waitcnt lgkmcnt(4)
	v_pk_fma_f32 v[46:47], v[50:51], v[40:41], v[46:47] op_sel:[0,1,0] op_sel_hi:[1,1,1]
	v_pk_fma_f32 v[48:49], v[52:53], v[40:41], v[48:49] op_sel:[0,1,0] op_sel_hi:[1,1,1]
	ds_read_b128 v[50:53], v45 offset:160
	s_waitcnt lgkmcnt(4)
	v_pk_fma_f32 v[46:47], v[56:57], v[38:39], v[46:47] op_sel:[0,1,0] op_sel_hi:[1,1,1]
	v_pk_fma_f32 v[48:49], v[58:59], v[38:39], v[48:49] op_sel:[0,1,0] op_sel_hi:[1,1,1]
	ds_read_b128 v[56:59], v45 offset:192
	s_waitcnt lgkmcnt(4)
	v_pk_fma_f32 v[46:47], v[60:61], v[36:37], v[46:47] op_sel:[0,1,0] op_sel_hi:[1,1,1]
	v_pk_fma_f32 v[48:49], v[62:63], v[36:37], v[48:49] op_sel:[0,1,0] op_sel_hi:[1,1,1]
	ds_read_b128 v[60:63], v45 offset:224
	s_waitcnt lgkmcnt(4)
	v_pk_fma_f32 v[46:47], v[64:65], v[36:37], v[46:47] op_sel_hi:[1,0,1]
	v_pk_fma_f32 v[48:49], v[66:67], v[36:37], v[48:49] op_sel_hi:[1,0,1]
	ds_read_b128 v[64:67], v45 offset:256
	s_waitcnt lgkmcnt(4)
	v_pk_fma_f32 v[46:47], v[68:69], v[34:35], v[46:47] op_sel:[0,1,0] op_sel_hi:[1,1,1]
	v_pk_fma_f32 v[48:49], v[70:71], v[34:35], v[48:49] op_sel:[0,1,0] op_sel_hi:[1,1,1]
	ds_read_b128 v[68:71], v45 offset:288
	s_waitcnt lgkmcnt(4)
	v_pk_fma_f32 v[46:47], v[50:51], v[34:35], v[46:47] op_sel_hi:[1,0,1]
	v_pk_fma_f32 v[48:49], v[52:53], v[34:35], v[48:49] op_sel_hi:[1,0,1]
	ds_read_b128 v[50:53], v45 offset:320
	s_waitcnt lgkmcnt(4)
	v_pk_fma_f32 v[46:47], v[56:57], v[32:33], v[46:47] op_sel:[0,1,0] op_sel_hi:[1,1,1]
	v_pk_fma_f32 v[48:49], v[58:59], v[32:33], v[48:49] op_sel:[0,1,0] op_sel_hi:[1,1,1]
	ds_read_b128 v[56:59], v45 offset:352
	s_waitcnt lgkmcnt(4)
	v_pk_fma_f32 v[46:47], v[60:61], v[32:33], v[46:47] op_sel_hi:[1,0,1]
	v_pk_fma_f32 v[48:49], v[62:63], v[32:33], v[48:49] op_sel_hi:[1,0,1]
	ds_read_b128 v[60:63], v45 offset:384
	s_waitcnt lgkmcnt(4)
	v_pk_fma_f32 v[46:47], v[64:65], v[42:43], v[46:47] op_sel_hi:[1,0,1]
	v_pk_fma_f32 v[48:49], v[66:67], v[42:43], v[48:49] op_sel_hi:[1,0,1]
	ds_read_b128 v[64:67], v45 offset:416
	s_waitcnt lgkmcnt(4)
	v_pk_fma_f32 v[46:47], v[68:69], v[44:45], v[46:47] op_sel_hi:[1,0,1]
	v_pk_fma_f32 v[48:49], v[70:71], v[44:45], v[48:49] op_sel_hi:[1,0,1]
	ds_read_b128 v[68:71], v45 offset:448
	s_waitcnt lgkmcnt(4)
	v_pk_fma_f32 v[46:47], v[50:51], v[42:43], v[46:47] op_sel:[0,1,0] op_sel_hi:[1,1,1]
	v_pk_fma_f32 v[48:49], v[52:53], v[42:43], v[48:49] op_sel:[0,1,0] op_sel_hi:[1,1,1]
	ds_read_b128 v[50:53], v45 offset:480
	s_waitcnt lgkmcnt(4)
	v_pk_fma_f32 v[46:47], v[56:57], v[40:41], v[46:47] op_sel_hi:[1,0,1]
	v_pk_fma_f32 v[48:49], v[58:59], v[40:41], v[48:49] op_sel_hi:[1,0,1]
	ds_read_b128 v[56:59], v45 offset:512
	s_waitcnt lgkmcnt(4)
	v_pk_fma_f32 v[46:47], v[60:61], v[38:39], v[46:47] op_sel_hi:[1,0,1]
	v_pk_fma_f32 v[48:49], v[62:63], v[38:39], v[48:49] op_sel_hi:[1,0,1]
	ds_read_b128 v[60:63], v45 offset:544
	s_waitcnt lgkmcnt(4)
	v_pk_fma_f32 v[46:47], v[64:65], v[26:27], v[46:47] op_sel_hi:[1,0,1]
	v_pk_fma_f32 v[48:49], v[66:67], v[26:27], v[48:49] op_sel_hi:[1,0,1]
	ds_read_b128 v[64:67], v45 offset:576
	s_waitcnt lgkmcnt(4)
	v_pk_fma_f32 v[46:47], v[68:69], v[26:27], v[46:47] op_sel:[0,1,0] op_sel_hi:[1,1,1]
	v_pk_fma_f32 v[48:49], v[70:71], v[26:27], v[48:49] op_sel:[0,1,0] op_sel_hi:[1,1,1]
	ds_read_b128 v[68:71], v45 offset:608
	s_waitcnt lgkmcnt(4)
	v_pk_fma_f32 v[46:47], v[50:51], v[28:29], v[46:47] op_sel_hi:[1,0,1]
	v_pk_fma_f32 v[48:49], v[52:53], v[28:29], v[48:49] op_sel_hi:[1,0,1]
	ds_read_b128 v[50:53], v45 offset:640
	s_waitcnt lgkmcnt(4)
	v_pk_fma_f32 v[46:47], v[56:57], v[24:25], v[46:47] op_sel_hi:[1,0,1]
	v_pk_fma_f32 v[48:49], v[58:59], v[24:25], v[48:49] op_sel_hi:[1,0,1]
	ds_read_b128 v[56:59], v45 offset:672
	s_waitcnt lgkmcnt(4)
	v_pk_fma_f32 v[46:47], v[60:61], v[28:29], v[46:47] op_sel:[0,1,0] op_sel_hi:[1,1,1]
	v_pk_fma_f32 v[48:49], v[62:63], v[28:29], v[48:49] op_sel:[0,1,0] op_sel_hi:[1,1,1]
	ds_read_b128 v[60:63], v45 offset:704
	s_waitcnt lgkmcnt(4)
	v_pk_fma_f32 v[46:47], v[64:65], v[30:31], v[46:47] op_sel_hi:[1,0,1]
	v_pk_fma_f32 v[48:49], v[66:67], v[30:31], v[48:49] op_sel_hi:[1,0,1]
	ds_read_b128 v[64:67], v45 offset:736
	s_waitcnt lgkmcnt(4)
	v_pk_fma_f32 v[46:47], v[68:69], v[30:31], v[46:47] op_sel:[0,1,0] op_sel_hi:[1,1,1]
	v_pk_fma_f32 v[48:49], v[70:71], v[30:31], v[48:49] op_sel:[0,1,0] op_sel_hi:[1,1,1]
	ds_read_b128 v[68:71], v45 offset:768
	s_waitcnt lgkmcnt(4)
	v_pk_fma_f32 v[46:47], v[50:51], v[24:25], v[46:47] op_sel:[0,1,0] op_sel_hi:[1,1,1]
	v_pk_fma_f32 v[48:49], v[52:53], v[24:25], v[48:49] op_sel:[0,1,0] op_sel_hi:[1,1,1]
	ds_read_b128 v[50:53], v45 offset:800
	s_waitcnt lgkmcnt(4)
	v_pk_fma_f32 v[46:47], v[56:57], v[18:19], v[46:47] op_sel_hi:[1,0,1]
	v_pk_fma_f32 v[48:49], v[58:59], v[18:19], v[48:49] op_sel_hi:[1,0,1]
	ds_read_b128 v[56:59], v45 offset:832
	s_waitcnt lgkmcnt(4)
	v_pk_fma_f32 v[46:47], v[60:61], v[18:19], v[46:47] op_sel:[0,1,0] op_sel_hi:[1,1,1]
	v_pk_fma_f32 v[48:49], v[62:63], v[18:19], v[48:49] op_sel:[0,1,0] op_sel_hi:[1,1,1]
	ds_read_b128 v[60:63], v45 offset:864
	s_waitcnt lgkmcnt(4)
	v_pk_fma_f32 v[46:47], v[64:65], v[20:21], v[46:47] op_sel_hi:[1,0,1]
	v_pk_fma_f32 v[48:49], v[66:67], v[20:21], v[48:49] op_sel_hi:[1,0,1]
	ds_read_b128 v[64:67], v45 offset:896
	s_waitcnt lgkmcnt(4)
	v_pk_fma_f32 v[46:47], v[68:69], v[16:17], v[46:47] op_sel_hi:[1,0,1]
	v_pk_fma_f32 v[48:49], v[70:71], v[16:17], v[48:49] op_sel_hi:[1,0,1]
	ds_read_b128 v[68:71], v45 offset:928
	s_waitcnt lgkmcnt(4)
	v_pk_fma_f32 v[46:47], v[50:51], v[20:21], v[46:47] op_sel:[0,1,0] op_sel_hi:[1,1,1]
	v_pk_fma_f32 v[48:49], v[52:53], v[20:21], v[48:49] op_sel:[0,1,0] op_sel_hi:[1,1,1]
	ds_read_b128 v[50:53], v45 offset:960
	s_waitcnt lgkmcnt(4)
	v_pk_fma_f32 v[46:47], v[56:57], v[22:23], v[46:47] op_sel_hi:[1,0,1]
	v_pk_fma_f32 v[48:49], v[58:59], v[22:23], v[48:49] op_sel_hi:[1,0,1]
	ds_read_b128 v[56:59], v45 offset:992
	s_waitcnt lgkmcnt(4)
	v_pk_fma_f32 v[46:47], v[60:61], v[22:23], v[46:47] op_sel:[0,1,0] op_sel_hi:[1,1,1]
	v_pk_fma_f32 v[48:49], v[62:63], v[22:23], v[48:49] op_sel:[0,1,0] op_sel_hi:[1,1,1]
	ds_read_b128 v[60:63], v45 offset:1024
	s_waitcnt lgkmcnt(4)
	v_pk_fma_f32 v[46:47], v[64:65], v[16:17], v[46:47] op_sel:[0,1,0] op_sel_hi:[1,1,1]
	v_pk_fma_f32 v[48:49], v[66:67], v[16:17], v[48:49] op_sel:[0,1,0] op_sel_hi:[1,1,1]
	ds_read_b128 v[64:67], v45 offset:1056
	s_waitcnt lgkmcnt(4)
	v_pk_fma_f32 v[46:47], v[68:69], v[10:11], v[46:47] op_sel_hi:[1,0,1]
	v_pk_fma_f32 v[48:49], v[70:71], v[10:11], v[48:49] op_sel_hi:[1,0,1]
	ds_read_b128 v[68:71], v45 offset:1088
	s_waitcnt lgkmcnt(4)
	v_pk_fma_f32 v[46:47], v[50:51], v[10:11], v[46:47] op_sel:[0,1,0] op_sel_hi:[1,1,1]
	v_pk_fma_f32 v[48:49], v[52:53], v[10:11], v[48:49] op_sel:[0,1,0] op_sel_hi:[1,1,1]
	ds_read_b128 v[50:53], v45 offset:1120
	s_waitcnt lgkmcnt(4)
	v_pk_fma_f32 v[46:47], v[56:57], v[12:13], v[46:47] op_sel_hi:[1,0,1]
	v_pk_fma_f32 v[48:49], v[58:59], v[12:13], v[48:49] op_sel_hi:[1,0,1]
	ds_read_b128 v[56:59], v45 offset:1152
	s_waitcnt lgkmcnt(4)
	v_pk_fma_f32 v[46:47], v[60:61], v[6:7], v[46:47] op_sel:[0,1,0] op_sel_hi:[1,1,1]
	v_pk_fma_f32 v[48:49], v[62:63], v[6:7], v[48:49] op_sel:[0,1,0] op_sel_hi:[1,1,1]
	ds_read_b128 v[60:63], v45 offset:1184
	s_waitcnt lgkmcnt(4)
	v_pk_fma_f32 v[46:47], v[64:65], v[12:13], v[46:47] op_sel:[0,1,0] op_sel_hi:[1,1,1]
	v_pk_fma_f32 v[48:49], v[66:67], v[12:13], v[48:49] op_sel:[0,1,0] op_sel_hi:[1,1,1]
	ds_read_b128 v[64:67], v45 offset:1216
	s_waitcnt lgkmcnt(4)
	v_pk_fma_f32 v[46:47], v[68:69], v[14:15], v[46:47] op_sel_hi:[1,0,1]
	v_pk_fma_f32 v[48:49], v[70:71], v[14:15], v[48:49] op_sel_hi:[1,0,1]
	s_waitcnt lgkmcnt(3)
	v_pk_fma_f32 v[46:47], v[50:51], v[14:15], v[46:47] op_sel:[0,1,0] op_sel_hi:[1,1,1]
	v_pk_fma_f32 v[48:49], v[52:53], v[14:15], v[48:49] op_sel:[0,1,0] op_sel_hi:[1,1,1]
	s_waitcnt lgkmcnt(2)
	v_pk_fma_f32 v[46:47], v[56:57], v[8:9], v[46:47] op_sel:[0,1,0] op_sel_hi:[1,1,1]
	v_pk_fma_f32 v[48:49], v[58:59], v[8:9], v[48:49] op_sel:[0,1,0] op_sel_hi:[1,1,1]
	s_waitcnt lgkmcnt(1)
	v_pk_fma_f32 v[46:47], v[60:61], v[8:9], v[46:47] op_sel_hi:[1,0,1]
	v_pk_fma_f32 v[48:49], v[62:63], v[8:9], v[48:49] op_sel_hi:[1,0,1]
	s_waitcnt lgkmcnt(0)
	v_pk_fma_f32 v[46:47], v[64:65], v[6:7], v[46:47] op_sel_hi:[1,0,1]
	v_pk_fma_f32 v[48:49], v[66:67], v[6:7], v[48:49] op_sel_hi:[1,0,1]
	v_mul_f32_e32 v46, 0xf800000, v46
	v_mul_f32_e32 v47, 0xf800000, v47
	v_mul_f32_e32 v48, 0xf800000, v48
	v_mul_f32_e32 v49, 0xf800000, v49
	global_store_dword v3, v46, s[6:7] offset:0
	global_store_dword v3, v47, s[6:7] offset:512
	global_store_dword v3, v48, s[6:7] offset:1024
	global_store_dword v3, v49, s[6:7] offset:1536
	s_mov_b64 s[4:5], 0

	.amdhsa_kernel _Z11prep_kernelPKfS0_S0_S0_S0_S0_S0_S0_PhPf
		.amdhsa_group_segment_fixed_size 1280
		.amdhsa_private_segment_fixed_size 0
		.amdhsa_kernarg_size 80
		.amdhsa_user_sgpr_count 2
		.amdhsa_user_sgpr_dispatch_ptr 0
		.amdhsa_user_sgpr_queue_ptr 0
		.amdhsa_user_sgpr_kernarg_segment_ptr 1
		.amdhsa_user_sgpr_dispatch_id 0
		.amdhsa_user_sgpr_kernarg_preload_length 0
		.amdhsa_user_sgpr_kernarg_preload_offset 0
		.amdhsa_user_sgpr_private_segment_size 0
		.amdhsa_uses_dynamic_stack 0
		.amdhsa_enable_private_segment 0
		.amdhsa_system_sgpr_workgroup_id_x 1
		.amdhsa_system_sgpr_workgroup_id_y 0
		.amdhsa_system_sgpr_workgroup_id_z 0
		.amdhsa_system_sgpr_workgroup_info 0
		.amdhsa_system_vgpr_workitem_id 0
		.amdhsa_next_free_vgpr 72
		.amdhsa_next_free_sgpr 24
		.amdhsa_accum_offset 72
		.amdhsa_reserve_vcc 1
		.amdhsa_float_round_mode_32 0
		.amdhsa_float_round_mode_16_64 0
		.amdhsa_float_denorm_mode_32 3
		.amdhsa_float_denorm_mode_16_64 3
		.amdhsa_dx10_clamp 1
		.amdhsa_ieee_mode 1
		.amdhsa_fp16_overflow 0
		.amdhsa_tg_split 0
		.amdhsa_exception_fp_ieee_invalid_op 0
		.amdhsa_exception_fp_denorm_src 0
		.amdhsa_exception_fp_ieee_div_zero 0
		.amdhsa_exception_fp_ieee_overflow 0
		.amdhsa_exception_fp_ieee_underflow 0
		.amdhsa_exception_fp_ieee_inexact 0
		.amdhsa_exception_int_div_zero 0
	.end_amdhsa_kernel

amdhsa.kernels:
  - .agpr_count:     0
    .args:
      - .actual_access:  read_only
        .address_space:  global
        .offset:         0
        .size:           8
        .value_kind:     global_buffer
      - .actual_access:  read_only
        .address_space:  global
        .offset:         8
        .size:           8
        .value_kind:     global_buffer
      - .actual_access:  read_only
        .address_space:  global
        .offset:         16
        .size:           8
        .value_kind:     global_buffer
      - .actual_access:  read_only
        .address_space:  global
        .offset:         24
        .size:           8
        .value_kind:     global_buffer
      - .actual_access:  read_only
        .address_space:  global
        .offset:         32
        .size:           8
        .value_kind:     global_buffer
      - .actual_access:  read_only
        .address_space:  global
        .offset:         40
        .size:           8
        .value_kind:     global_buffer
      - .actual_access:  read_only
        .address_space:  global
        .offset:         48
        .size:           8
        .value_kind:     global_buffer
      - .actual_access:  read_only
        .address_space:  global
        .offset:         56
        .size:           8
        .value_kind:     global_buffer
      - .actual_access:  write_only
        .address_space:  global
        .offset:         64
        .size:           8
        .value_kind:     global_buffer
      - .actual_access:  write_only
        .address_space:  global
        .offset:         72
        .size:           8
        .value_kind:     global_buffer
    .group_segment_fixed_size: 1280
    .kernarg_segment_align: 8
    .kernarg_segment_size: 80
    .language:       OpenCL C
    .language_version:
      - 2
      - 0
    .max_flat_workgroup_size: 256
    .name:           _Z11prep_kernelPKfS0_S0_S0_S0_S0_S0_S0_PhPf
    .private_segment_fixed_size: 0
    .sgpr_count:     30
    .sgpr_spill_count: 0
    .symbol:         _Z11prep_kernelPKfS0_S0_S0_S0_S0_S0_S0_PhPf.kd
    .uniform_work_group_size: 1
    .uses_dynamic_stack: false
    .vgpr_count:     72
    .vgpr_spill_count: 0
    .wavefront_size: 64
  - .agpr_count:     0
    .args:
      - .actual_access:  read_only
        .address_space:  global
        .offset:         0
        .size:           8
        .value_kind:     global_buffer
      - .address_space:  global
        .offset:         8
        .size:           8
        .value_kind:     global_buffer
      - .actual_access:  read_only
        .address_space:  global
        .offset:         16
        .size:           8
        .value_kind:     global_buffer
      - .actual_access:  read_only
        .address_space:  global
        .offset:         24
        .size:           8
        .value_kind:     global_buffer
      - .actual_access:  write_only
        .address_space:  global
        .offset:         32
        .size:           8
        .value_kind:     global_buffer
    .group_segment_fixed_size: 0
    .kernarg_segment_align: 8
    .kernarg_segment_size: 40
    .language:       OpenCL C
    .language_version:
      - 2
      - 0
    .max_flat_workgroup_size: 512
    .name:           _Z13render_kernelPKfPKhS0_S0_Pf
    .private_segment_fixed_size: 0
    .sgpr_count:     28
    .sgpr_spill_count: 0
    .symbol:         _Z13render_kernelPKfPKhS0_S0_Pf.kd
    .uniform_work_group_size: 1
    .uses_dynamic_stack: false
    .vgpr_count:     256
    .vgpr_spill_count: 0
    .wavefront_size: 64
